# P7 inner loop: selection-mask application and row-max tree spread over the 15 PV MFMA gaps (6 VALU per gap, in place on the QK accumulators) instead of hipcc's placement behind the last sched_barrier
# speedup vs baseline: 1.0107x; 1.0107x over previous
.LBB0_1727:
	ds_read_b128 v[66:69], v203 offset:49152
	ds_read_b128 v[82:85], v203 offset:57344
	ds_read_b128 v[234:237], v204 offset:49152
	ds_read_b128 v[238:241], v204 offset:57344
	v_add_f32_e32 v216, 0, v225
	v_add_f32_e32 v216, v227, v216
	s_waitcnt lgkmcnt(3)
	v_mfma_f32_32x32x16_bf16 v[66:81], v[66:69], v[126:129], 0
	v_add_f32_e32 v216, v228, v216
	v_add_f32_e32 v216, v230, v216
	v_add_f32_e32 v216, v231, v216
	v_add_f32_e32 v216, v232, v216
	v_add_f32_e32 v216, v226, v216
	v_add_f32_e32 v216, v229, v216
	v_add_f32_e32 v216, v195, v216
	s_waitcnt lgkmcnt(2)
	v_mfma_f32_32x32x16_bf16 v[82:97], v[82:85], v[126:129], 0
	v_add_f32_e32 v216, v221, v216
	v_add_f32_e32 v216, v222, v216
	v_add_f32_e32 v216, v223, v216
	v_exp_f32_e32 v144, v144
	v_add_f32_e32 v216, v194, v216
	v_exp_f32_e32 v145, v145
	v_add_f32_e32 v216, v219, v216
	s_waitcnt lgkmcnt(1)
	v_mfma_f32_32x32x16_bf16 v[66:81], v[234:237], v[122:125], v[66:81]
	v_exp_f32_e32 v142, v142
	v_add_f32_e32 v216, v220, v216
	v_exp_f32_e32 v143, v143
	v_add_f32_e32 v216, v224, v216
	v_exp_f32_e32 v140, v140
	v_add_f32_e32 v216, v144, v216
	v_exp_f32_e32 v141, v141
	s_waitcnt lgkmcnt(0)
	v_mfma_f32_32x32x16_bf16 v[82:97], v[238:241], v[122:125], v[82:97]
	ds_read_b128 v[234:237], v205 offset:49152
	ds_read_b128 v[238:241], v205 offset:57344
	v_add_f32_e32 v216, v145, v216
	v_exp_f32_e32 v138, v138
	v_add_f32_e32 v216, v142, v216
	v_exp_f32_e32 v139, v139
	v_add_f32_e32 v216, v143, v216
	v_exp_f32_e32 v136, v136
	s_waitcnt lgkmcnt(1)
	v_mfma_f32_32x32x16_bf16 v[66:81], v[234:237], v[118:121], v[66:81]
	v_add_f32_e32 v216, v140, v216
	v_exp_f32_e32 v137, v137
	v_add_f32_e32 v216, v141, v216
	v_exp_f32_e32 v134, v134
	v_add_f32_e32 v216, v138, v216
	v_exp_f32_e32 v135, v135
	v_add_f32_e32 v216, v139, v216
	s_waitcnt lgkmcnt(0)
	v_mfma_f32_32x32x16_bf16 v[82:97], v[238:241], v[118:121], v[82:97]
	ds_read_b128 v[234:237], v206 offset:49152
	ds_read_b128 v[238:241], v206 offset:57344
	v_exp_f32_e32 v132, v132
	v_add_f32_e32 v216, v136, v216
	v_exp_f32_e32 v133, v133
	v_add_f32_e32 v216, v137, v216
	v_exp_f32_e32 v130, v130
	v_add_f32_e32 v216, v134, v216
	s_waitcnt lgkmcnt(1)
	v_mfma_f32_32x32x16_bf16 v[66:81], v[234:237], v[114:117], v[66:81]
	v_exp_f32_e32 v131, v131
	v_add_f32_e32 v216, v135, v216
	v_add_f32_e32 v216, v132, v216
	v_add_f32_e32 v216, v133, v216
	v_add_f32_e32 v216, v130, v216
	v_add_f32_e32 v216, v131, v216
	v_mov_b32_e32 v217, v216
	s_waitcnt lgkmcnt(0)
	v_mfma_f32_32x32x16_bf16 v[82:97], v[238:241], v[114:117], v[82:97]
	ds_read_b128 v[234:237], v207 offset:49152
	ds_read_b128 v[238:241], v207 offset:57344
	v_cvt_pk_bf16_f32 v218, v144, v145
	v_permlane32_swap_b32_e32 v216, v217
	s_waitcnt lgkmcnt(1)
	v_mfma_f32_32x32x16_bf16 v[66:81], v[234:237], v[110:113], v[66:81]
	s_waitcnt lgkmcnt(0)
	v_mfma_f32_32x32x16_bf16 v[82:97], v[238:241], v[110:113], v[82:97]
	ds_read_b128 v[234:237], v208 offset:49152
	ds_read_b128 v[238:241], v208 offset:57344
	s_waitcnt lgkmcnt(1)
	v_mfma_f32_32x32x16_bf16 v[66:81], v[234:237], v[106:109], v[66:81]
	s_waitcnt lgkmcnt(0)
	v_mfma_f32_32x32x16_bf16 v[82:97], v[238:241], v[106:109], v[82:97]
	ds_read_b128 v[234:237], v209 offset:49152
	ds_read_b128 v[238:241], v209 offset:57344
	s_waitcnt lgkmcnt(1)
	v_mfma_f32_32x32x16_bf16 v[66:81], v[234:237], v[102:105], v[66:81]
	s_waitcnt lgkmcnt(0)
	v_mfma_f32_32x32x16_bf16 v[82:97], v[238:241], v[102:105], v[82:97]
	ds_read_b128 v[234:237], v210 offset:49152
	ds_read_b128 v[238:241], v210 offset:57344
	s_waitcnt lgkmcnt(1)
	v_mfma_f32_32x32x16_bf16 v[66:81], v[234:237], v[98:101], v[66:81]
	v_cvt_pk_bf16_f32 v235, v228, v230
	v_cvt_pk_bf16_f32 v237, v226, v229
	v_cvt_pk_bf16_f32 v226, v195, v221
	v_cvt_pk_bf16_f32 v228, v194, v219
	v_cvt_pk_bf16_f32 v229, v220, v224
	v_cvt_pk_bf16_f32 v219, v142, v143
	v_cvt_pk_bf16_f32 v220, v140, v141
	s_waitcnt lgkmcnt(0)
	v_mfma_f32_32x32x16_bf16 v[82:97], v[238:241], v[98:101], v[82:97]
	v_cvt_pk_bf16_f32 v221, v138, v139
	v_cvt_pk_bf16_f32 v234, v225, v227
	v_cvt_pk_bf16_f32 v236, v231, v232
	v_cvt_pk_bf16_f32 v227, v222, v223
	v_permlane32_swap_b32_e32 v218, v220
	v_permlane32_swap_b32_e32 v219, v221
	v_cvt_pk_bf16_f32 v222, v136, v137
	v_cvt_pk_bf16_f32 v223, v134, v135
	v_cvt_pk_bf16_f32 v224, v132, v133
	v_cvt_pk_bf16_f32 v225, v130, v131
	v_permlane32_swap_b32_e32 v234, v236
	v_permlane32_swap_b32_e32 v235, v237
	v_permlane32_swap_b32_e32 v226, v228
	v_permlane32_swap_b32_e32 v227, v229
	v_permlane32_swap_b32_e32 v222, v224
	v_permlane32_swap_b32_e32 v223, v225
	v_lshl_add_u64 v[194:195], s[44:45], 0, v[188:189]
	v_add_co_u32_e32 v134, vcc, s36, v194
	s_nop 1
	v_addc_co_u32_e32 v135, vcc, 0, v195, vcc
	v_add_co_u32_e32 v138, vcc, s37, v194
	s_nop 1
	v_addc_co_u32_e32 v139, vcc, 0, v195, vcc
	global_load_dwordx4 v[130:133], v[134:135], off offset:2560
	s_nop 0
	global_load_dwordx4 v[134:137], v[134:135], off offset:2048
	s_nop 0
	global_load_dwordx4 v[142:145], v[138:139], off offset:2560
	s_nop 0
	global_load_dwordx4 v[138:141], v[138:139], off offset:2048
	ds_read_b64_tr_b16 v[230:231], v147 offset:0
	ds_read_b64_tr_b16 v[232:233], v147 offset:0x800
	ds_read_b64_tr_b16 v[238:239], v147 offset:0x1000
	ds_read_b64_tr_b16 v[240:241], v147 offset:0x1800
	ds_read_b64_tr_b16 v[242:243], v147 offset:0x2000
	ds_read_b64_tr_b16 v[244:245], v147 offset:0x2800
	ds_read_b64_tr_b16 v[246:247], v147 offset:0x3000
	ds_read_b64_tr_b16 v[248:249], v147 offset:0x3800
	s_waitcnt lgkmcnt(0)
	s_nop 0
	v_mfma_f32_32x32x16_bf16 v[50:65], v[234:237], v[230:233], v[50:65]
	ds_read_b64_tr_b16 v[230:231], v147 offset:0x200
	ds_read_b64_tr_b16 v[232:233], v147 offset:0xa00
	v_lshrrev_b32_e32 v184, v1, v184
	v_lshrrev_b32_e32 v185, v1, v185
	v_bfe_i32 v254, v184, 0, 1
	v_bitop3_b32 v66, v66, s34, v254 bitop3:0xe4
	v_bfe_i32 v254, v184, 1, 1
	v_bitop3_b32 v67, v67, s34, v254 bitop3:0xe4
	v_mfma_f32_32x32x16_bf16 v[50:65], v[226:229], v[238:241], v[50:65]
	ds_read_b64_tr_b16 v[238:239], v147 offset:0x1200
	ds_read_b64_tr_b16 v[240:241], v147 offset:0x1a00
	v_max_f32_e32 v255, v67, v67
	v_max_f32_e32 v254, v66, v66
	v_max_f32_e32 v255, v254, v255
	v_bfe_i32 v254, v184, 2, 1
	v_bitop3_b32 v68, v68, s34, v254 bitop3:0xe4
	v_bfe_i32 v254, v184, 3, 1
	v_mfma_f32_32x32x16_bf16 v[50:65], v[218:221], v[242:245], v[50:65]
	ds_read_b64_tr_b16 v[242:243], v147 offset:0x2200
	ds_read_b64_tr_b16 v[244:245], v147 offset:0x2a00
	ds_read_b64_tr_b16 v[250:251], v147 offset:0x3200
	ds_read_b64_tr_b16 v[252:253], v147 offset:0x3a00
	v_bitop3_b32 v69, v69, s34, v254 bitop3:0xe4
	v_max3_f32 v255, v255, v68, v69
	v_bfe_i32 v254, v184, 8, 1
	v_bitop3_b32 v70, v70, s34, v254 bitop3:0xe4
	v_bfe_i32 v254, v184, 9, 1
	v_bitop3_b32 v71, v71, s34, v254 bitop3:0xe4
	s_waitcnt lgkmcnt(0)
	v_mfma_f32_32x32x16_bf16 v[50:65], v[222:225], v[246:249], v[50:65]
	v_max3_f32 v255, v255, v70, v71
	v_bfe_i32 v254, v184, 10, 1
	v_bitop3_b32 v72, v72, s34, v254 bitop3:0xe4
	v_bfe_i32 v254, v184, 11, 1
	v_bitop3_b32 v73, v73, s34, v254 bitop3:0xe4
	v_max3_f32 v255, v255, v72, v73
	v_mfma_f32_32x32x16_bf16 v[34:49], v[234:237], v[230:233], v[34:49]
	ds_read_b64_tr_b16 v[230:231], v147 offset:0x400
	ds_read_b64_tr_b16 v[232:233], v147 offset:0xc00
	v_bfe_i32 v254, v184, 16, 1
	v_bitop3_b32 v74, v74, s34, v254 bitop3:0xe4
	v_bfe_i32 v254, v184, 17, 1
	v_bitop3_b32 v75, v75, s34, v254 bitop3:0xe4
	v_max3_f32 v255, v255, v74, v75
	v_bfe_i32 v254, v184, 18, 1
	v_mfma_f32_32x32x16_bf16 v[34:49], v[226:229], v[238:241], v[34:49]
	ds_read_b64_tr_b16 v[238:239], v147 offset:0x1400
	ds_read_b64_tr_b16 v[240:241], v147 offset:0x1c00
	v_bitop3_b32 v76, v76, s34, v254 bitop3:0xe4
	v_bfe_i32 v254, v184, 19, 1
	v_bitop3_b32 v77, v77, s34, v254 bitop3:0xe4
	v_max3_f32 v255, v255, v76, v77
	v_bfe_i32 v254, v184, 24, 1
	v_bitop3_b32 v78, v78, s34, v254 bitop3:0xe4
	v_mfma_f32_32x32x16_bf16 v[34:49], v[218:221], v[242:245], v[34:49]
	ds_read_b64_tr_b16 v[242:243], v147 offset:0x2400
	ds_read_b64_tr_b16 v[244:245], v147 offset:0x2c00
	ds_read_b64_tr_b16 v[246:247], v147 offset:0x3400
	ds_read_b64_tr_b16 v[248:249], v147 offset:0x3c00
	v_bfe_i32 v254, v184, 25, 1
	v_bitop3_b32 v79, v79, s34, v254 bitop3:0xe4
	v_max3_f32 v255, v255, v78, v79
	v_bfe_i32 v254, v184, 26, 1
	v_bitop3_b32 v80, v80, s34, v254 bitop3:0xe4
	v_bfe_i32 v254, v184, 27, 1
	s_waitcnt lgkmcnt(0)
	v_mfma_f32_32x32x16_bf16 v[34:49], v[222:225], v[250:253], v[34:49]
	v_bitop3_b32 v81, v81, s34, v254 bitop3:0xe4
	v_max3_f32 v255, v255, v80, v81
	v_bfe_i32 v254, v185, 0, 1
	v_bitop3_b32 v82, v82, s34, v254 bitop3:0xe4
	v_bfe_i32 v254, v185, 1, 1
	v_bitop3_b32 v83, v83, s34, v254 bitop3:0xe4
	v_mfma_f32_32x32x16_bf16 v[18:33], v[234:237], v[230:233], v[18:33]
	ds_read_b64_tr_b16 v[230:231], v147 offset:0x600
	ds_read_b64_tr_b16 v[232:233], v147 offset:0xe00
	v_max3_f32 v255, v255, v82, v83
	v_bfe_i32 v254, v185, 2, 1
	v_bitop3_b32 v84, v84, s34, v254 bitop3:0xe4
	v_bfe_i32 v254, v185, 3, 1
	v_bitop3_b32 v85, v85, s34, v254 bitop3:0xe4
	v_max3_f32 v255, v255, v84, v85
	v_mfma_f32_32x32x16_bf16 v[18:33], v[226:229], v[238:241], v[18:33]
	ds_read_b64_tr_b16 v[238:239], v147 offset:0x1600
	ds_read_b64_tr_b16 v[240:241], v147 offset:0x1e00
	v_bfe_i32 v254, v185, 8, 1
	v_bitop3_b32 v86, v86, s34, v254 bitop3:0xe4
	v_bfe_i32 v254, v185, 9, 1
	v_bitop3_b32 v87, v87, s34, v254 bitop3:0xe4
	v_max3_f32 v255, v255, v86, v87
	v_bfe_i32 v254, v185, 10, 1
	v_mfma_f32_32x32x16_bf16 v[18:33], v[218:221], v[242:245], v[18:33]
	ds_read_b64_tr_b16 v[242:243], v147 offset:0x2600
	ds_read_b64_tr_b16 v[244:245], v147 offset:0x2e00
	ds_read_b64_tr_b16 v[250:251], v147 offset:0x3600
	ds_read_b64_tr_b16 v[252:253], v147 offset:0x3e00
	v_bitop3_b32 v88, v88, s34, v254 bitop3:0xe4
	v_bfe_i32 v254, v185, 11, 1
	v_bitop3_b32 v89, v89, s34, v254 bitop3:0xe4
	v_max3_f32 v255, v255, v88, v89
	v_bfe_i32 v254, v185, 16, 1
	v_bitop3_b32 v90, v90, s34, v254 bitop3:0xe4
	s_waitcnt lgkmcnt(0)
	v_mfma_f32_32x32x16_bf16 v[18:33], v[222:225], v[246:249], v[18:33]
	v_bfe_i32 v254, v185, 17, 1
	v_bitop3_b32 v91, v91, s34, v254 bitop3:0xe4
	v_max3_f32 v255, v255, v90, v91
	v_bfe_i32 v254, v185, 18, 1
	v_bitop3_b32 v92, v92, s34, v254 bitop3:0xe4
	v_bfe_i32 v254, v185, 19, 1
	v_mfma_f32_32x32x16_bf16 v[2:17], v[234:237], v[230:233], v[2:17]
	v_bitop3_b32 v93, v93, s34, v254 bitop3:0xe4
	v_max3_f32 v255, v255, v92, v93
	v_bfe_i32 v254, v185, 24, 1
	v_bitop3_b32 v94, v94, s34, v254 bitop3:0xe4
	v_bfe_i32 v254, v185, 25, 1
	v_bitop3_b32 v95, v95, s34, v254 bitop3:0xe4
	v_mfma_f32_32x32x16_bf16 v[2:17], v[226:229], v[238:241], v[2:17]
	v_max3_f32 v255, v255, v94, v95
	v_bfe_i32 v254, v185, 26, 1
	v_bitop3_b32 v96, v96, s34, v254 bitop3:0xe4
	v_bfe_i32 v254, v185, 27, 1
	v_bitop3_b32 v97, v97, s34, v254 bitop3:0xe4
	v_max3_f32 v255, v255, v96, v97
	v_mfma_f32_32x32x16_bf16 v[2:17], v[218:221], v[242:245], v[2:17]
	v_mov_b32_e32 v254, v255
	s_nop 1
	v_permlane32_swap_b32_e32 v255, v254
	v_max_f32_e32 v254, v254, v254
	v_max_f32_e32 v255, v255, v255
	v_max_f32_e32 v255, v255, v254
	v_max_f32_e32 v184, v215, v215
	v_sub_f32_e32 v254, v255, v215
	v_max_f32_e32 v255, v184, v255
	v_mfma_f32_32x32x16_bf16 v[2:17], v[222:225], v[250:253], v[2:17]
	v_sub_f32_e32 v184, v215, v255
	v_mul_f32_e32 v184, 0x3e0293ee, v184
	v_exp_f32_e32 v184, v184
	v_cmp_ge_f32_e32 vcc, s35, v254
	s_cmp_eq_u64 vcc, exec
	s_cselect_b64 s[6:7], -1, 0
	s_barrier
	s_waitcnt vmcnt(0)
	v_cndmask_b32_e64 v218, v184, 1.0, s[6:7]
	v_cmp_gt_f32_e32 vcc, 1.0, v218
	s_waitcnt vmcnt(3)
	ds_write_b128 v199, v[130:133]
	s_waitcnt vmcnt(1)
	ds_write_b128 v200, v[142:145]
	ds_write_b128 v201, v[134:137] offset:32768
	s_waitcnt vmcnt(0)
	ds_write_b128 v202, v[138:141] offset:32768
	s_cbranch_vccz .LBB0_1731
	s_and_saveexec_b64 s[28:29], s[4:5]
	ds_write_b32 v196, v218 offset:128
	s_or_b64 exec, exec, s[28:29]
	s_waitcnt lgkmcnt(0)
	ds_read_b128 v[130:133], v198 offset:224
	ds_read_b128 v[134:137], v198 offset:192
	ds_read_b128 v[138:141], v198 offset:160
	ds_read_b128 v[142:145], v198 offset:128
	s_waitcnt lgkmcnt(3)
	v_pk_mul_f32 v[64:65], v[64:65], v[132:133]
	s_waitcnt lgkmcnt(2)
	v_pk_mul_f32 v[60:61], v[60:61], v[136:137]
	s_waitcnt lgkmcnt(1)
	v_pk_mul_f32 v[56:57], v[56:57], v[140:141]
	s_waitcnt lgkmcnt(0)
	v_pk_mul_f32 v[52:53], v[52:53], v[144:145]
	v_pk_mul_f32 v[62:63], v[62:63], v[130:131]
	v_pk_mul_f32 v[58:59], v[58:59], v[134:135]
	v_pk_mul_f32 v[54:55], v[54:55], v[138:139]
	v_pk_mul_f32 v[50:51], v[50:51], v[142:143]
	v_pk_mul_f32 v[48:49], v[48:49], v[132:133]
	v_pk_mul_f32 v[44:45], v[44:45], v[136:137]
	v_pk_mul_f32 v[40:41], v[40:41], v[140:141]
	v_pk_mul_f32 v[36:37], v[36:37], v[144:145]
	v_pk_mul_f32 v[46:47], v[46:47], v[130:131]
	v_pk_mul_f32 v[42:43], v[42:43], v[134:135]
	v_pk_mul_f32 v[38:39], v[38:39], v[138:139]
	v_pk_mul_f32 v[34:35], v[34:35], v[142:143]
	v_pk_mul_f32 v[32:33], v[32:33], v[132:133]
	v_pk_mul_f32 v[28:29], v[28:29], v[136:137]
	v_pk_mul_f32 v[24:25], v[24:25], v[140:141]
	v_pk_mul_f32 v[20:21], v[20:21], v[144:145]
	v_pk_mul_f32 v[30:31], v[30:31], v[130:131]
	v_pk_mul_f32 v[26:27], v[26:27], v[134:135]
	v_pk_mul_f32 v[22:23], v[22:23], v[138:139]
	v_pk_mul_f32 v[18:19], v[18:19], v[142:143]
	v_pk_mul_f32 v[16:17], v[16:17], v[132:133]
	v_pk_mul_f32 v[12:13], v[12:13], v[136:137]
	v_pk_mul_f32 v[8:9], v[8:9], v[140:141]
	v_pk_mul_f32 v[4:5], v[4:5], v[144:145]
	v_pk_mul_f32 v[14:15], v[14:15], v[130:131]
	v_pk_mul_f32 v[10:11], v[10:11], v[134:135]
	v_pk_mul_f32 v[6:7], v[6:7], v[138:139]
	v_pk_mul_f32 v[2:3], v[2:3], v[142:143]
.LBB0_1731:
	v_cndmask_b32_e64 v215, v255, v215, s[6:7]
	v_mul_f32_e32 v221, 0xbe0293ee, v215
	v_fmamk_f32 v66, v66, 0x3e0293ee, v221
	v_fmamk_f32 v67, v67, 0x3e0293ee, v221
	v_fmamk_f32 v68, v68, 0x3e0293ee, v221
	v_fmamk_f32 v69, v69, 0x3e0293ee, v221
	v_fmamk_f32 v70, v70, 0x3e0293ee, v221
	v_fmamk_f32 v71, v71, 0x3e0293ee, v221
	v_fmamk_f32 v72, v72, 0x3e0293ee, v221
	v_fmamk_f32 v73, v73, 0x3e0293ee, v221
	v_fmamk_f32 v74, v74, 0x3e0293ee, v221
	v_fmamk_f32 v75, v75, 0x3e0293ee, v221
	v_fmamk_f32 v76, v76, 0x3e0293ee, v221
	v_fmamk_f32 v77, v77, 0x3e0293ee, v221
	v_fmamk_f32 v78, v78, 0x3e0293ee, v221
	v_fmamk_f32 v79, v79, 0x3e0293ee, v221
	v_fmamk_f32 v80, v80, 0x3e0293ee, v221
	v_fmamk_f32 v81, v81, 0x3e0293ee, v221
	v_exp_f32_e32 v138, v66
	v_exp_f32_e32 v140, v67
	v_exp_f32_e32 v141, v68
	v_exp_f32_e32 v143, v69
	v_exp_f32_e32 v144, v70
	v_exp_f32_e32 v145, v71
	v_exp_f32_e32 v139, v72
	v_exp_f32_e32 v142, v73
	v_exp_f32_e32 v131, v74
	v_exp_f32_e32 v134, v75
	v_exp_f32_e32 v135, v76
	v_exp_f32_e32 v137, v77
	v_exp_f32_e32 v130, v78
	v_exp_f32_e32 v132, v79
	v_exp_f32_e32 v133, v80
	v_exp_f32_e32 v136, v81
	s_add_i32 s12, s12, 1
	v_fmamk_f32 v228, v82, 0x3e0293ee, v221
	v_fmamk_f32 v229, v83, 0x3e0293ee, v221
	v_fmamk_f32 v230, v84, 0x3e0293ee, v221
	v_fmamk_f32 v231, v85, 0x3e0293ee, v221
	v_fmamk_f32 v232, v86, 0x3e0293ee, v221
	v_fmamk_f32 v220, v87, 0x3e0293ee, v221
	v_fmamk_f32 v222, v88, 0x3e0293ee, v221
	v_fmamk_f32 v223, v89, 0x3e0293ee, v221
	v_fmamk_f32 v224, v90, 0x3e0293ee, v221
	v_fmamk_f32 v225, v91, 0x3e0293ee, v221
	v_fmamk_f32 v226, v92, 0x3e0293ee, v221
	v_fmamk_f32 v227, v93, 0x3e0293ee, v221
	v_fmamk_f32 v219, v94, 0x3e0293ee, v221
	v_fmamk_f32 v233, v95, 0x3e0293ee, v221
	v_fmamk_f32 v234, v96, 0x3e0293ee, v221
	v_fmac_f32_e32 v221, 0x3e0293ee, v97
	s_cmp_gt_u32 s12, s54
	v_mov_b64_e32 v[184:185], 0
	s_waitcnt lgkmcnt(0)
	s_barrier
	s_cbranch_scc1 .LBB0_1733
	v_add_co_u32_e32 v66, vcc, 0x98a98000, v192
	s_nop 1
	v_addc_co_u32_e32 v67, vcc, 0, v193, vcc
	global_load_dwordx2 v[184:185], v[66:67], off offset:24
.LBB0_1733:
	ds_read_b128 v[66:69], v203 offset:32768
	ds_read_b128 v[70:73], v203 offset:40960
	ds_read_b128 v[236:239], v204 offset:32768
	ds_read_b128 v[240:243], v204 offset:40960
	v_add_f32_e32 v192, 0, v138
	v_add_f32_e32 v192, v140, v192
	s_waitcnt lgkmcnt(3)
	v_mfma_f32_32x32x16_bf16 v[82:97], v[66:69], v[126:129], 0
	v_add_f32_e32 v192, v141, v192
	v_add_f32_e32 v192, v143, v192
	v_add_f32_e32 v192, v144, v192
	v_add_f32_e32 v192, v145, v192
	v_add_f32_e32 v192, v139, v192
	v_add_f32_e32 v192, v142, v192
	v_add_f32_e32 v192, v131, v192
	s_waitcnt lgkmcnt(2)
	v_mfma_f32_32x32x16_bf16 v[66:81], v[70:73], v[126:129], 0
	v_add_f32_e32 v192, v134, v192
	v_add_f32_e32 v192, v135, v192
	v_add_f32_e32 v192, v137, v192
	v_exp_f32_e32 v228, v228
	v_add_f32_e32 v192, v130, v192
	v_exp_f32_e32 v229, v229
	v_add_f32_e32 v192, v132, v192
	s_waitcnt lgkmcnt(1)
	v_mfma_f32_32x32x16_bf16 v[82:97], v[236:239], v[122:125], v[82:97]
	v_exp_f32_e32 v230, v230
	v_add_f32_e32 v192, v133, v192
	v_exp_f32_e32 v231, v231
	v_add_f32_e32 v192, v136, v192
	v_exp_f32_e32 v232, v232
	v_add_f32_e32 v192, v228, v192
	v_exp_f32_e32 v235, v220
	s_waitcnt lgkmcnt(0)
	v_mfma_f32_32x32x16_bf16 v[66:81], v[240:243], v[122:125], v[66:81]
	ds_read_b128 v[236:239], v205 offset:32768
	ds_read_b128 v[240:243], v205 offset:40960
	v_add_f32_e32 v192, v229, v192
	v_add_f32_e32 v192, v230, v192
	v_add_f32_e32 v192, v231, v192
	v_add_f32_e32 v192, v232, v192
	v_add_f32_e32 v192, v235, v192
	v_exp_f32_e32 v219, v219
	s_waitcnt lgkmcnt(1)
	v_mfma_f32_32x32x16_bf16 v[82:97], v[236:239], v[118:121], v[82:97]
	v_exp_f32_e32 v244, v221
	v_cvt_pk_bf16_f32 v220, v138, v140
	v_cvt_pk_bf16_f32 v221, v141, v143
	v_cvt_pk_bf16_f32 v228, v228, v229
	v_cvt_pk_bf16_f32 v229, v230, v231
	v_cvt_pk_bf16_f32 v230, v232, v235
	s_nop 1
	v_permlane32_swap_b32_e32 v228, v230
	s_waitcnt lgkmcnt(0)
	v_mfma_f32_32x32x16_bf16 v[66:81], v[240:243], v[118:121], v[66:81]
	ds_read_b128 v[236:239], v206 offset:32768
	ds_read_b128 v[240:243], v206 offset:40960
	s_waitcnt lgkmcnt(1)
	v_mfma_f32_32x32x16_bf16 v[82:97], v[236:239], v[114:117], v[82:97]
	s_waitcnt lgkmcnt(0)
	v_mfma_f32_32x32x16_bf16 v[66:81], v[240:243], v[114:117], v[66:81]
	ds_read_b128 v[236:239], v207 offset:32768
	ds_read_b128 v[240:243], v207 offset:40960
	s_waitcnt lgkmcnt(1)
	v_mfma_f32_32x32x16_bf16 v[82:97], v[236:239], v[110:113], v[82:97]
	s_waitcnt lgkmcnt(0)
	v_mfma_f32_32x32x16_bf16 v[66:81], v[240:243], v[110:113], v[66:81]
	ds_read_b128 v[236:239], v208 offset:32768
	ds_read_b128 v[240:243], v208 offset:40960
	s_waitcnt lgkmcnt(1)
	v_mfma_f32_32x32x16_bf16 v[82:97], v[236:239], v[106:109], v[82:97]
	s_waitcnt lgkmcnt(0)
	v_mfma_f32_32x32x16_bf16 v[66:81], v[240:243], v[106:109], v[66:81]
	ds_read_b128 v[236:239], v209 offset:32768
	ds_read_b128 v[240:243], v209 offset:40960
	s_waitcnt lgkmcnt(1)
	v_mfma_f32_32x32x16_bf16 v[82:97], v[236:239], v[102:105], v[82:97]
	s_waitcnt lgkmcnt(0)
	v_mfma_f32_32x32x16_bf16 v[66:81], v[240:243], v[102:105], v[66:81]
	ds_read_b128 v[236:239], v210 offset:32768
	ds_read_b128 v[240:243], v210 offset:40960
	s_waitcnt lgkmcnt(1)
	v_mfma_f32_32x32x16_bf16 v[82:97], v[236:239], v[98:101], v[82:97]
	v_exp_f32_e32 v236, v222
	v_exp_f32_e32 v237, v223
	v_exp_f32_e32 v238, v224
	v_exp_f32_e32 v239, v225
	v_add_f32_e32 v192, v236, v192
	v_add_f32_e32 v192, v237, v192
	v_add_f32_e32 v192, v238, v192
	s_waitcnt lgkmcnt(0)
	v_mfma_f32_32x32x16_bf16 v[66:81], v[240:243], v[98:101], v[66:81]
	v_exp_f32_e32 v240, v226
	v_exp_f32_e32 v241, v227
	v_exp_f32_e32 v242, v233
	v_add_f32_e32 v192, v239, v192
	v_exp_f32_e32 v243, v234
	v_add_f32_e32 v192, v240, v192
	v_add_f32_e32 v192, v241, v192
	v_add_f32_e32 v192, v219, v192
	v_add_f32_e32 v192, v242, v192
	v_add_f32_e32 v192, v243, v192
	v_add_f32_e32 v192, v244, v192
	v_mov_b32_e32 v193, v192
	s_nop 1
	v_permlane32_swap_b32_e32 v192, v193
	v_cvt_pk_bf16_f32 v222, v144, v145
	v_cvt_pk_bf16_f32 v223, v139, v142
	v_cvt_pk_bf16_f32 v224, v131, v134
	v_cvt_pk_bf16_f32 v225, v135, v137
	v_cvt_pk_bf16_f32 v226, v130, v132
	v_cvt_pk_bf16_f32 v227, v133, v136
	v_cvt_pk_bf16_f32 v231, v236, v237
	v_cvt_pk_bf16_f32 v232, v238, v239
	v_cvt_pk_bf16_f32 v233, v240, v241
	v_cvt_pk_bf16_f32 v234, v219, v242
	v_cvt_pk_bf16_f32 v235, v243, v244
	v_permlane32_swap_b32_e32 v220, v222
	v_permlane32_swap_b32_e32 v221, v223
	v_permlane32_swap_b32_e32 v224, v226
	v_permlane32_swap_b32_e32 v225, v227
	v_permlane32_swap_b32_e32 v229, v231
	v_permlane32_swap_b32_e32 v232, v234
	v_permlane32_swap_b32_e32 v233, v235
	v_add_co_u32_e32 v134, vcc, s38, v194
	s_nop 1
	v_addc_co_u32_e32 v135, vcc, 0, v195, vcc
	v_add_co_u32_e32 v138, vcc, s39, v194
	s_nop 1
	v_addc_co_u32_e32 v139, vcc, 0, v195, vcc
	global_load_dwordx4 v[130:133], v[134:135], off offset:2560
	s_nop 0
	global_load_dwordx4 v[134:137], v[134:135], off offset:2048
	s_nop 0
	global_load_dwordx4 v[142:145], v[138:139], off offset:2560
	s_nop 0
	global_load_dwordx4 v[138:141], v[138:139], off offset:2048
	ds_read_b64_tr_b16 v[236:237], v197 offset:0
	ds_read_b64_tr_b16 v[238:239], v197 offset:0x800
	ds_read_b64_tr_b16 v[240:241], v197 offset:0x1000
	ds_read_b64_tr_b16 v[242:243], v197 offset:0x1800
	ds_read_b64_tr_b16 v[244:245], v197 offset:0x2000
	ds_read_b64_tr_b16 v[246:247], v197 offset:0x2800
	ds_read_b64_tr_b16 v[248:249], v197 offset:0x3000
	ds_read_b64_tr_b16 v[250:251], v197 offset:0x3800
	s_waitcnt lgkmcnt(0)
	s_nop 0
	v_mfma_f32_32x32x16_bf16 v[50:65], v[220:223], v[236:239], v[50:65]
	ds_read_b64_tr_b16 v[236:237], v197 offset:0x200
	ds_read_b64_tr_b16 v[238:239], v197 offset:0xa00
	v_lshrrev_b32_e32 v190, v1, v190
	v_bfe_i32 v194, v190, 0, 1
	v_bitop3_b32 v82, v82, s34, v194 bitop3:0xe4
	v_bfe_i32 v194, v190, 1, 1
	v_bitop3_b32 v83, v83, s34, v194 bitop3:0xe4
	v_max_f32_e32 v219, v83, v83
	v_mfma_f32_32x32x16_bf16 v[50:65], v[224:227], v[240:243], v[50:65]
	ds_read_b64_tr_b16 v[240:241], v197 offset:0x1200
	ds_read_b64_tr_b16 v[242:243], v197 offset:0x1a00
	v_max_f32_e32 v194, v82, v82
	v_max_f32_e32 v219, v194, v219
	v_bfe_i32 v194, v190, 2, 1
	v_bitop3_b32 v84, v84, s34, v194 bitop3:0xe4
	v_bfe_i32 v194, v190, 3, 1
	v_bitop3_b32 v85, v85, s34, v194 bitop3:0xe4
	v_mfma_f32_32x32x16_bf16 v[50:65], v[228:231], v[244:247], v[50:65]
	ds_read_b64_tr_b16 v[244:245], v197 offset:0x2200
	ds_read_b64_tr_b16 v[246:247], v197 offset:0x2a00
	ds_read_b64_tr_b16 v[252:253], v197 offset:0x3200
	ds_read_b64_tr_b16 v[254:255], v197 offset:0x3a00
	v_max3_f32 v219, v219, v84, v85
	v_bfe_i32 v194, v190, 8, 1
	v_bitop3_b32 v86, v86, s34, v194 bitop3:0xe4
	v_bfe_i32 v194, v190, 9, 1
	v_bitop3_b32 v87, v87, s34, v194 bitop3:0xe4
	v_max3_f32 v219, v219, v86, v87
	s_waitcnt lgkmcnt(0)
	v_mfma_f32_32x32x16_bf16 v[50:65], v[232:235], v[248:251], v[50:65]
	v_bfe_i32 v194, v190, 10, 1
	v_bitop3_b32 v88, v88, s34, v194 bitop3:0xe4
	v_bfe_i32 v194, v190, 11, 1
	v_bitop3_b32 v89, v89, s34, v194 bitop3:0xe4
	v_max3_f32 v219, v219, v88, v89
	v_bfe_i32 v194, v190, 16, 1
	v_mfma_f32_32x32x16_bf16 v[34:49], v[220:223], v[236:239], v[34:49]
	ds_read_b64_tr_b16 v[236:237], v197 offset:0x400
	ds_read_b64_tr_b16 v[238:239], v197 offset:0xc00
	v_bitop3_b32 v90, v90, s34, v194 bitop3:0xe4
	v_bfe_i32 v194, v190, 17, 1
	v_bitop3_b32 v91, v91, s34, v194 bitop3:0xe4
	v_max3_f32 v219, v219, v90, v91
	v_bfe_i32 v194, v190, 18, 1
	v_bitop3_b32 v92, v92, s34, v194 bitop3:0xe4
	v_mfma_f32_32x32x16_bf16 v[34:49], v[224:227], v[240:243], v[34:49]
	ds_read_b64_tr_b16 v[240:241], v197 offset:0x1400
	ds_read_b64_tr_b16 v[242:243], v197 offset:0x1c00
	v_bfe_i32 v194, v190, 19, 1
	v_bitop3_b32 v93, v93, s34, v194 bitop3:0xe4
	v_max3_f32 v219, v219, v92, v93
	v_bfe_i32 v194, v190, 24, 1
	v_bitop3_b32 v94, v94, s34, v194 bitop3:0xe4
	v_bfe_i32 v194, v190, 25, 1
	v_mfma_f32_32x32x16_bf16 v[34:49], v[228:231], v[244:247], v[34:49]
	ds_read_b64_tr_b16 v[244:245], v197 offset:0x2400
	ds_read_b64_tr_b16 v[246:247], v197 offset:0x2c00
	ds_read_b64_tr_b16 v[248:249], v197 offset:0x3400
	ds_read_b64_tr_b16 v[250:251], v197 offset:0x3c00
	v_bitop3_b32 v95, v95, s34, v194 bitop3:0xe4
	v_max3_f32 v219, v219, v94, v95
	v_bfe_i32 v194, v190, 26, 1
	v_bitop3_b32 v96, v96, s34, v194 bitop3:0xe4
	v_bfe_i32 v194, v190, 27, 1
	v_bitop3_b32 v97, v97, s34, v194 bitop3:0xe4
	s_waitcnt lgkmcnt(0)
	v_mfma_f32_32x32x16_bf16 v[34:49], v[232:235], v[252:255], v[34:49]
	v_max3_f32 v219, v219, v96, v97
	v_lshrrev_b32_e32 v191, v1, v191
	v_bfe_i32 v195, v191, 0, 1
	v_bitop3_b32 v66, v66, s34, v195 bitop3:0xe4
	v_bfe_i32 v195, v191, 1, 1
	v_bitop3_b32 v67, v67, s34, v195 bitop3:0xe4
	v_mfma_f32_32x32x16_bf16 v[18:33], v[220:223], v[236:239], v[18:33]
	ds_read_b64_tr_b16 v[236:237], v197 offset:0x600
	ds_read_b64_tr_b16 v[238:239], v197 offset:0xe00
	v_max3_f32 v219, v219, v66, v67
	v_bfe_i32 v195, v191, 2, 1
	v_bitop3_b32 v68, v68, s34, v195 bitop3:0xe4
	v_bfe_i32 v195, v191, 3, 1
	v_bitop3_b32 v69, v69, s34, v195 bitop3:0xe4
	v_max3_f32 v219, v219, v68, v69
	v_mfma_f32_32x32x16_bf16 v[18:33], v[224:227], v[240:243], v[18:33]
	ds_read_b64_tr_b16 v[240:241], v197 offset:0x1600
	ds_read_b64_tr_b16 v[242:243], v197 offset:0x1e00
	v_bfe_i32 v195, v191, 8, 1
	v_bitop3_b32 v70, v70, s34, v195 bitop3:0xe4
	v_bfe_i32 v195, v191, 9, 1
	v_bitop3_b32 v71, v71, s34, v195 bitop3:0xe4
	v_max3_f32 v219, v219, v70, v71
	v_bfe_i32 v195, v191, 10, 1
	v_mfma_f32_32x32x16_bf16 v[18:33], v[228:231], v[244:247], v[18:33]
	ds_read_b64_tr_b16 v[244:245], v197 offset:0x2600
	ds_read_b64_tr_b16 v[246:247], v197 offset:0x2e00
	ds_read_b64_tr_b16 v[252:253], v197 offset:0x3600
	ds_read_b64_tr_b16 v[254:255], v197 offset:0x3e00
	v_bitop3_b32 v72, v72, s34, v195 bitop3:0xe4
	v_bfe_i32 v195, v191, 11, 1
	v_bitop3_b32 v73, v73, s34, v195 bitop3:0xe4
	v_max3_f32 v219, v219, v72, v73
	v_bfe_i32 v195, v191, 16, 1
	v_bitop3_b32 v74, v74, s34, v195 bitop3:0xe4
	s_waitcnt lgkmcnt(0)
	v_mfma_f32_32x32x16_bf16 v[18:33], v[232:235], v[248:251], v[18:33]
	v_bfe_i32 v195, v191, 17, 1
	v_bitop3_b32 v75, v75, s34, v195 bitop3:0xe4
	v_max3_f32 v219, v219, v74, v75
	v_bfe_i32 v195, v191, 18, 1
	v_bitop3_b32 v76, v76, s34, v195 bitop3:0xe4
	v_bfe_i32 v195, v191, 19, 1
	v_mfma_f32_32x32x16_bf16 v[2:17], v[220:223], v[236:239], v[2:17]
	v_bitop3_b32 v77, v77, s34, v195 bitop3:0xe4
	v_max3_f32 v219, v219, v76, v77
	v_bfe_i32 v195, v191, 24, 1
	v_bitop3_b32 v78, v78, s34, v195 bitop3:0xe4
	v_bfe_i32 v195, v191, 25, 1
	v_bitop3_b32 v79, v79, s34, v195 bitop3:0xe4
	v_mfma_f32_32x32x16_bf16 v[2:17], v[224:227], v[240:243], v[2:17]
	v_max3_f32 v219, v219, v78, v79
	v_bfe_i32 v195, v191, 26, 1
	v_bitop3_b32 v80, v80, s34, v195 bitop3:0xe4
	v_bfe_i32 v195, v191, 27, 1
	v_bitop3_b32 v81, v81, s34, v195 bitop3:0xe4
	v_max3_f32 v190, v219, v80, v81
	v_mfma_f32_32x32x16_bf16 v[2:17], v[228:231], v[244:247], v[2:17]
	v_mov_b32_e32 v191, v190
	s_nop 1
	v_permlane32_swap_b32_e32 v190, v191
	v_max_f32_e32 v191, v191, v191
	v_max_f32_e32 v190, v190, v190
	v_max_f32_e32 v190, v190, v191
	v_max_f32_e32 v191, v215, v215
	v_max_f32_e32 v191, v191, v190
	v_mfma_f32_32x32x16_bf16 v[2:17], v[232:235], v[252:255], v[2:17]
	v_sub_f32_e32 v194, v190, v215
	v_sub_f32_e32 v190, v215, v191
	v_mul_f32_e32 v190, 0x3e0293ee, v190
	v_exp_f32_e32 v190, v190
	v_cmp_ge_f32_e32 vcc, s35, v194
	s_cmp_eq_u64 vcc, exec
	s_cselect_b64 s[6:7], -1, 0
	s_barrier
	s_waitcnt vmcnt(0)
	v_cndmask_b32_e64 v190, v190, 1.0, s[6:7]
	v_cmp_gt_f32_e32 vcc, 1.0, v190
	s_waitcnt vmcnt(3)
	ds_write_b128 v199, v[130:133] offset:16384
	s_waitcnt vmcnt(1)
	ds_write_b128 v200, v[142:145] offset:16384
	ds_write_b128 v201, v[134:137] offset:49152
	s_waitcnt vmcnt(0)
	ds_write_b128 v202, v[138:141] offset:49152
	s_cbranch_vccz .LBB0_1737
	s_and_saveexec_b64 s[28:29], s[4:5]
	ds_write_b32 v196, v190 offset:128
	s_or_b64 exec, exec, s[28:29]
	s_waitcnt lgkmcnt(0)
	ds_read_b128 v[130:133], v198 offset:224
	ds_read_b128 v[134:137], v198 offset:192
	ds_read_b128 v[138:141], v198 offset:160
	ds_read_b128 v[142:145], v198 offset:128
	s_waitcnt lgkmcnt(3)
	v_pk_mul_f32 v[64:65], v[64:65], v[132:133]
	s_waitcnt lgkmcnt(2)
	v_pk_mul_f32 v[60:61], v[60:61], v[136:137]
	s_waitcnt lgkmcnt(1)
	v_pk_mul_f32 v[56:57], v[56:57], v[140:141]
	s_waitcnt lgkmcnt(0)
	v_pk_mul_f32 v[52:53], v[52:53], v[144:145]
	v_pk_mul_f32 v[62:63], v[62:63], v[130:131]
	v_pk_mul_f32 v[58:59], v[58:59], v[134:135]
	v_pk_mul_f32 v[54:55], v[54:55], v[138:139]
	v_pk_mul_f32 v[50:51], v[50:51], v[142:143]
	v_pk_mul_f32 v[48:49], v[48:49], v[132:133]
	v_pk_mul_f32 v[44:45], v[44:45], v[136:137]
	v_pk_mul_f32 v[40:41], v[40:41], v[140:141]
	v_pk_mul_f32 v[36:37], v[36:37], v[144:145]
	v_pk_mul_f32 v[46:47], v[46:47], v[130:131]
	v_pk_mul_f32 v[42:43], v[42:43], v[134:135]
	v_pk_mul_f32 v[38:39], v[38:39], v[138:139]
	v_pk_mul_f32 v[34:35], v[34:35], v[142:143]
	v_pk_mul_f32 v[32:33], v[32:33], v[132:133]
	v_pk_mul_f32 v[28:29], v[28:29], v[136:137]
	v_pk_mul_f32 v[24:25], v[24:25], v[140:141]
	v_pk_mul_f32 v[20:21], v[20:21], v[144:145]
	v_pk_mul_f32 v[30:31], v[30:31], v[130:131]
	v_pk_mul_f32 v[26:27], v[26:27], v[134:135]
	v_pk_mul_f32 v[22:23], v[22:23], v[138:139]
	v_pk_mul_f32 v[18:19], v[18:19], v[142:143]
	v_pk_mul_f32 v[16:17], v[16:17], v[132:133]
	v_pk_mul_f32 v[12:13], v[12:13], v[136:137]
	v_pk_mul_f32 v[8:9], v[8:9], v[140:141]
	v_pk_mul_f32 v[4:5], v[4:5], v[144:145]
	v_pk_mul_f32 v[14:15], v[14:15], v[130:131]
	v_pk_mul_f32 v[10:11], v[10:11], v[134:135]
	v_pk_mul_f32 v[6:7], v[6:7], v[138:139]
	v_pk_mul_f32 v[2:3], v[2:3], v[142:143]
